# v34 + MLA row sums: the two accumulator-initialising adds with zero folded into the first real adds (2 VALU fewer per tile)
# speedup vs baseline: 1.0052x; 1.0037x over previous
; __device__ __forceinline__ unsigned cvt_pk_bf16(float lo, float hi) { unsigned r; asm volatile("v_cvt_pk_bf16_f32 %0, %1, %2" : "=v"(r) : "v"(lo), "v"(hi)); return r; }
; #define SFENCE() __builtin_amdgcn_sched_barrier(0)
; template <bool FOX>
; __device__ __forceinline__ void attn_unit(const Args& A, int b, int h, int qb, LAS char* shm, LAS float* dg) {
;     ...
;           const lds_cptr vp = vp0 + ((t - 1) % NS) * VSLOT; float sa = 0.f, sb = 0.f;
; #pragma unroll
;           for (int g = 0; g < 2 * NQ; ++g) {
;               if (!FOX && g == 0) c0 = __builtin_amdgcn_mfma_f32_32x32x16_bf16(kf[0], qr[0], negm, 0, 0, 0);
;               else if (!FOX && g == 1) c1 = __builtin_amdgcn_mfma_f32_32x32x16_bf16(kf[1], qr[0], negm, 0, 0, 0);
;               else if (g & 1) c1 = __builtin_amdgcn_mfma_f32_32x32x16_bf16(kf[g], qr[g >> 1], c1, 0, 0, 0); else c0 = __builtin_amdgcn_mfma_f32_32x32x16_bf16(kf[g], qr[g >> 1], c0, 0, 0, 0);
;               if (g < 8) { const int i = (g >> 1) + 4 * (g & 1); vlo[i] = vtr(vp + (i >> 2) * 4096 + (i & 3) * 1024); vhi[i] = vtr(vp + (i >> 2) * 4096 + (i & 3) * 1024 + 512);
;                   if (g < 4) { sa += pp0[4 * g]; sb += pp0[4 * g + 1]; sa += pp0[4 * g + 2]; sb += pp0[4 * g + 3]; } else { sa += pp1[4 * g - 16]; sb += pp1[4 * g - 15]; sa += pp1[4 * g - 14]; sb += pp1[4 * g - 13]; }
;                   asm volatile("" : "+v"(sa), "+v"(sb)); }
;               { constexpr int G0 = FOX ? 0 : 4; if (g >= G0) { const int q = 2 * (g - G0);
; #pragma unroll
;                   for (int k = 0; k < 2; ++k) { const int w = q + k; const unsigned pkd = w < 8 ? cvt_pk_bf16(pp0[2 * w], pp0[2 * w + 1]) : cvt_pk_bf16(pp1[2 * w - 16], pp1[2 * w - 15]); pw[w >> 2][w & 3] = pkd; } } }
;               SFENCE();
;           }
;           lrun += sa + sb; }
;         MASKONLY(t);
;         float rm; ROWMAX(rm);
;         bool resc = false;
;         if (__any(rm > THR)) { const float dl = fmaxf(rm, 0.f); mhat += dl;
; #pragma unroll
;             for (int r = 0; r < 16; ++r) { c0[r] -= dl; c1[r] -= dl; }
;             if constexpr (!FOX) {
; #pragma unroll
;                 for (int r = 0; r < 16; ++r) negm[r] = -mhat;
;                 asm volatile("" : "+v"(negm)); }
;             const float f = __builtin_amdgcn_exp2f(-dl); lrun *= f; if (hi == 0) wsf[r32] = f; resc = true; }
.LBB0_835:
	s_add_i32 s27, s42, 0x8000
	v_mfma_f32_32x32x16_bf16 v[114:129], v[206:209], v[138:141], v[82:97]
	s_and_b32 s27, s27, 0x6000
	v_add_u32_e32 v3, s27, v247
	ds_read_b64_tr_b16 v[206:207], v3 offset:49152
	ds_read_b64_tr_b16 v[208:209], v3 offset:49664
	v_add_f32_e32 v4, v69, v67
	v_add_f32_e32 v5, v68, v66
	v_mfma_f32_32x32x16_bf16 v[98:113], v[194:197], v[138:141], v[82:97]
	ds_read_b64_tr_b16 v[194:195], v3 offset:53248
	ds_read_b64_tr_b16 v[196:197], v3 offset:53760
	v_add_f32_e32 v4, v71, v4
	v_add_f32_e32 v5, v70, v5
	v_add_f32_e32 v4, v73, v4
	v_add_f32_e32 v5, v72, v5
	v_mfma_f32_32x32x16_bf16 v[114:129], v[202:205], v[142:145], v[114:129]
	ds_read_b64_tr_b16 v[202:203], v3 offset:50176
	ds_read_b64_tr_b16 v[204:205], v3 offset:50688
	v_add_f32_e32 v4, v75, v4
	v_add_f32_e32 v5, v74, v5
	v_add_f32_e32 v4, v77, v4
	v_add_f32_e32 v5, v76, v5
	v_mfma_f32_32x32x16_bf16 v[98:113], v[186:189], v[142:145], v[98:113]
	ds_read_b64_tr_b16 v[214:215], v3 offset:54272
	ds_read_b64_tr_b16 v[216:217], v3 offset:54784
	v_add_f32_e32 v4, v79, v4
	v_add_f32_e32 v5, v78, v5
	v_add_f32_e32 v4, v81, v4
	v_add_f32_e32 v5, v80, v5
	v_mfma_f32_32x32x16_bf16 v[114:129], v[198:201], v[146:149], v[114:129]
	ds_read_b64_tr_b16 v[210:211], v3 offset:51200
	ds_read_b64_tr_b16 v[212:213], v3 offset:51712
	v_add_f32_e32 v4, v51, v4
	v_add_f32_e32 v5, v50, v5
	v_add_f32_e32 v4, v53, v4
	v_add_f32_e32 v5, v52, v5
	v_mfma_f32_32x32x16_bf16 v[98:113], v[182:185], v[146:149], v[98:113]
	ds_read_b64_tr_b16 v[12:13], v3 offset:55296
	ds_read_b64_tr_b16 v[14:15], v3 offset:55808
	v_add_f32_e32 v4, v55, v4
	v_add_f32_e32 v5, v54, v5
	v_add_f32_e32 v4, v57, v4
	v_add_f32_e32 v5, v56, v5
	v_mfma_f32_32x32x16_bf16 v[114:129], v[190:193], v[150:153], v[114:129]
	ds_read_b64_tr_b16 v[8:9], v3 offset:52224
	ds_read_b64_tr_b16 v[10:11], v3 offset:52736
	v_add_f32_e32 v4, v59, v4
	v_add_f32_e32 v16, v61, v4
	v_add_f32_e32 v4, v58, v5
	v_add_f32_e32 v17, v60, v4
	v_mfma_f32_32x32x16_bf16 v[98:113], v[170:173], v[150:153], v[98:113]
	ds_read_b64_tr_b16 v[4:5], v3 offset:56320
	ds_read_b64_tr_b16 v[6:7], v3 offset:56832
	v_add_f32_e32 v3, v63, v16
	v_add_f32_e32 v16, v62, v17
	v_add_f32_e32 v3, v65, v3
	v_add_f32_e32 v16, v64, v16
	v_mfma_f32_32x32x16_bf16 v[114:129], v[178:181], v[154:157], v[114:129]
	v_cvt_pk_bf16_f32 v178, v50, v51
	v_cvt_pk_bf16_f32 v179, v52, v53
	v_cvt_pk_bf16_f32 v186, v66, v67
	v_cvt_pk_bf16_f32 v187, v68, v69
	v_mfma_f32_32x32x16_bf16 v[98:113], v[166:169], v[154:157], v[98:113]
	v_cvt_pk_bf16_f32 v180, v54, v55
	v_cvt_pk_bf16_f32 v181, v56, v57
	v_cvt_pk_bf16_f32 v188, v70, v71
	v_cvt_pk_bf16_f32 v189, v72, v73
	v_mfma_f32_32x32x16_bf16 v[114:129], v[174:177], v[158:161], v[114:129]
	v_cvt_pk_bf16_f32 v218, v58, v59
	v_cvt_pk_bf16_f32 v219, v60, v61
	v_cvt_pk_bf16_f32 v182, v74, v75
	v_cvt_pk_bf16_f32 v183, v76, v77
	v_mfma_f32_32x32x16_bf16 v[98:113], v[162:165], v[158:161], v[98:113]
	v_cvt_pk_bf16_f32 v220, v62, v63
	v_cvt_pk_bf16_f32 v221, v64, v65
	v_cvt_pk_bf16_f32 v184, v78, v79
	v_cvt_pk_bf16_f32 v185, v80, v81
	v_add_f32_e32 v3, v3, v16
	s_cmp_lg_u32 s98, 0
	s_cbranch_scc1 .Lmla_fixed_ref
	s_nop 9
	v_max_f32_e32 v16, v115, v115
	v_max_f32_e32 v17, v114, v114
	v_max_f32_e32 v16, v17, v16
	v_max3_f32 v17, v116, v117, v99
	v_max3_f32 v16, v16, v98, v100
	v_max3_f32 v16, v16, v101, v118
	v_max3_f32 v17, v17, v120, v121
	v_max3_f32 v16, v16, v119, v102
	v_max3_f32 v17, v17, v104, v105
	v_max3_f32 v16, v16, v103, v122
	v_max3_f32 v17, v17, v124, v125
	v_max3_f32 v16, v16, v123, v106
	v_max3_f32 v17, v17, v108, v109
	v_max3_f32 v16, v16, v107, v126
	v_max3_f32 v17, v17, v128, v129
	v_max3_f32 v16, v16, v127, v110
	v_max3_f32 v17, v17, v112, v113
	v_add_f32_e32 v246, v246, v3
	v_max3_f32 v3, v16, v111, v17
	v_mov_b32_e32 v16, v3
	s_nop 1
	v_permlane32_swap_b32_e32 v3, v16
	v_max_f32_e32 v16, v16, v16
	v_max_f32_e32 v3, v3, v3
	v_max_f32_e32 v3, v3, v16
	v_cmp_lt_f32_e32 vcc, s95, v3
	s_cmp_lg_u64 vcc, 0
	s_cselect_b64 s[60:61], -1, 0
	s_cbranch_vccz .LBB0_839
	v_max_f32_e32 v3, v3, v3
	v_max_f32_e32 v3, 0, v3
	v_exp_f32_e64 v16, -v3
	v_add_f32_e32 v249, v249, v3
	v_xor_b32_e32 v82, 0x80000000, v249
	v_mov_b32_e32 v83, v82
	v_mov_b32_e32 v84, v82
	v_mov_b32_e32 v85, v82
	v_mov_b32_e32 v86, v82
	v_mov_b32_e32 v87, v82
	v_mov_b32_e32 v88, v82
	v_mov_b32_e32 v89, v82
	v_mov_b32_e32 v90, v82
	v_mov_b32_e32 v91, v82
	v_mov_b32_e32 v92, v82
	v_mov_b32_e32 v93, v82
	v_mov_b32_e32 v94, v82
	v_mov_b32_e32 v95, v82
	v_mov_b32_e32 v96, v82
	v_mov_b32_e32 v97, v82
	s_and_saveexec_b64 s[64:65], s[24:25]
	ds_write_b32 v245, v16
	s_or_b64 exec, exec, s[64:65]
	v_sub_f32_e32 v129, v129, v3
	v_sub_f32_e32 v128, v128, v3
	v_sub_f32_e32 v127, v127, v3
	v_sub_f32_e32 v126, v126, v3
	v_sub_f32_e32 v125, v125, v3
	v_sub_f32_e32 v124, v124, v3
	v_sub_f32_e32 v123, v123, v3
	v_sub_f32_e32 v122, v122, v3
	v_sub_f32_e32 v121, v121, v3
	v_sub_f32_e32 v120, v120, v3
	v_sub_f32_e32 v119, v119, v3
	v_sub_f32_e32 v118, v118, v3
	v_sub_f32_e32 v117, v117, v3
	v_sub_f32_e32 v116, v116, v3
	v_sub_f32_e32 v115, v115, v3
	v_sub_f32_e32 v114, v114, v3
	v_sub_f32_e32 v113, v113, v3
	v_sub_f32_e32 v112, v112, v3
	v_sub_f32_e32 v111, v111, v3
	v_sub_f32_e32 v110, v110, v3
	v_sub_f32_e32 v109, v109, v3
	v_sub_f32_e32 v108, v108, v3
	v_sub_f32_e32 v107, v107, v3
	v_sub_f32_e32 v106, v106, v3
	v_sub_f32_e32 v105, v105, v3
	v_sub_f32_e32 v104, v104, v3
	v_sub_f32_e32 v103, v103, v3
	v_sub_f32_e32 v102, v102, v3
	v_sub_f32_e32 v101, v101, v3
	v_sub_f32_e32 v100, v100, v3
	v_sub_f32_e32 v99, v99, v3
	v_sub_f32_e32 v98, v98, v3
	v_mul_f32_e32 v246, v246, v16
	s_branch .LBB0_839

; template <bool FOX>
; __device__ __forceinline__ void attn_unit(const Args& A, int b, int h, int qb, LAS char* shm, LAS float* dg) {
;     ...
;     for (int t = 1; t < t_end; ++t) {
;         if (t == 1 && 4 < nti) ISSUE_K(t0 + 4, 0);
;         if (t + 4 < nti) ISSUE_K(t0 + t + 4, t % NS);
;         if (t + 2 < nti) ISSUE_V(t0 + t + 2, (t + 2) % NS);
;         SFENCE();
;         { if constexpr (!FOX) { if (t0 + t == tw_last + 1) {
; #pragma unroll
;                   for (int r = 0; r < 16; ++r) negm[r] = -INFINITY;
;                   asm volatile("" : "+v"(negm)); } }
;           const lds_cptr vp = vp0 + ((t - 1) % NS) * VSLOT; float sa = 0.f, sb = 0.f;
; #pragma unroll
;           for (int g = 0; g < 2 * NQ; ++g) {
;               if (!FOX && g == 0) c0 = __builtin_amdgcn_mfma_f32_32x32x16_bf16(kf[0], qr[0], negm, 0, 0, 0);
;               else if (!FOX && g == 1) c1 = __builtin_amdgcn_mfma_f32_32x32x16_bf16(kf[1], qr[0], negm, 0, 0, 0);
;               else if (g & 1) c1 = __builtin_amdgcn_mfma_f32_32x32x16_bf16(kf[g], qr[g >> 1], c1, 0, 0, 0); else c0 = __builtin_amdgcn_mfma_f32_32x32x16_bf16(kf[g], qr[g >> 1], c0, 0, 0, 0);
;               if (g < 8) { const int i = (g >> 1) + 4 * (g & 1); vlo[i] = vtr(vp + (i >> 2) * 4096 + (i & 3) * 1024); vhi[i] = vtr(vp + (i >> 2) * 4096 + (i & 3) * 1024 + 512);
;                   if (g < 4) { sa += pp0[4 * g]; sb += pp0[4 * g + 1]; sa += pp0[4 * g + 2]; sb += pp0[4 * g + 3]; } else { sa += pp1[4 * g - 16]; sb += pp1[4 * g - 15]; sa += pp1[4 * g - 14]; sb += pp1[4 * g - 13]; }
;                   asm volatile("" : "+v"(sa), "+v"(sb)); }
;               { constexpr int G0 = FOX ? 0 : 4; if (g >= G0) { const int q = 2 * (g - G0);
; #pragma unroll
;                   for (int k = 0; k < 2; ++k) { const int w = q + k; const unsigned pkd = w < 8 ? cvt_pk_bf16(pp0[2 * w], pp0[2 * w + 1]) : cvt_pk_bf16(pp1[2 * w - 16], pp1[2 * w - 15]); pw[w >> 2][w & 3] = pkd; } } }
;               SFENCE();
;           }
;           lrun += sa + sb; }
;         MASKONLY(t);
;         float rm; ROWMAX(rm);
;         bool resc = false;
;         if (__any(rm > THR)) { const float dl = fmaxf(rm, 0.f); mhat += dl;
; #pragma unroll
;             for (int r = 0; r < 16; ++r) { c0[r] -= dl; c1[r] -= dl; }
;             if constexpr (!FOX) {
; #pragma unroll
;                 for (int r = 0; r < 16; ++r) negm[r] = -mhat;
.Lmla_ss1_in:
	s_mov_b32 m0, s52
	s_nop 0
	global_load_lds_dwordx4 v240, s[46:47]
	s_add_i32 m0, s52, 0x2000
	s_nop 0
	global_load_lds_dwordx4 v240, s[98:99]
	s_mov_b32 m0, s53
	s_nop 0
	global_load_lds_dwordx4 v240, s[60:61]
	s_waitcnt lgkmcnt(0)
	s_add_i32 s27, s42, 0x8000
	v_mfma_f32_32x32x16_bf16 v[114:129], v[206:209], v[138:141], v[82:97]
	s_and_b32 s27, s27, 0x6000
	s_add_u32 s42, s42, 0x2000
	s_addc_u32 s43, s43, 0
	v_add_u32_e32 v3, s27, v247
	ds_read_b64_tr_b16 v[206:207], v3 offset:49152
	ds_read_b64_tr_b16 v[208:209], v3 offset:49664
	v_add_f32_e32 v4, v69, v67
	v_add_f32_e32 v5, v68, v66
	v_mfma_f32_32x32x16_bf16 v[98:113], v[194:197], v[138:141], v[82:97]
	ds_read_b64_tr_b16 v[194:195], v3 offset:53248
	ds_read_b64_tr_b16 v[196:197], v3 offset:53760
	v_add_f32_e32 v4, v71, v4
	v_add_f32_e32 v5, v70, v5
	v_add_f32_e32 v4, v73, v4
	v_add_f32_e32 v5, v72, v5
	v_mfma_f32_32x32x16_bf16 v[114:129], v[202:205], v[142:145], v[114:129]
	ds_read_b64_tr_b16 v[202:203], v3 offset:50176
	ds_read_b64_tr_b16 v[204:205], v3 offset:50688
	v_add_f32_e32 v4, v75, v4
	v_add_f32_e32 v5, v74, v5
	v_add_f32_e32 v4, v77, v4
	v_add_f32_e32 v5, v76, v5
	v_mfma_f32_32x32x16_bf16 v[98:113], v[186:189], v[142:145], v[98:113]
	ds_read_b64_tr_b16 v[214:215], v3 offset:54272
	ds_read_b64_tr_b16 v[216:217], v3 offset:54784
	v_add_f32_e32 v4, v79, v4
	v_add_f32_e32 v5, v78, v5
	v_add_f32_e32 v4, v81, v4
	v_add_f32_e32 v5, v80, v5
	v_mfma_f32_32x32x16_bf16 v[114:129], v[198:201], v[146:149], v[114:129]
	ds_read_b64_tr_b16 v[210:211], v3 offset:51200
	ds_read_b64_tr_b16 v[212:213], v3 offset:51712
	v_add_f32_e32 v4, v51, v4
	v_add_f32_e32 v5, v50, v5
	v_add_f32_e32 v4, v53, v4
	v_add_f32_e32 v5, v52, v5
	v_mfma_f32_32x32x16_bf16 v[98:113], v[182:185], v[146:149], v[98:113]
	ds_read_b64_tr_b16 v[12:13], v3 offset:55296
	ds_read_b64_tr_b16 v[14:15], v3 offset:55808
	v_add_f32_e32 v4, v55, v4
	v_add_f32_e32 v5, v54, v5
	v_add_f32_e32 v4, v57, v4
	v_add_f32_e32 v5, v56, v5
	v_mfma_f32_32x32x16_bf16 v[114:129], v[190:193], v[150:153], v[114:129]
	ds_read_b64_tr_b16 v[8:9], v3 offset:52224
	ds_read_b64_tr_b16 v[10:11], v3 offset:52736
	v_add_f32_e32 v4, v59, v4
	v_add_f32_e32 v16, v61, v4
	v_add_f32_e32 v4, v58, v5
	v_add_f32_e32 v17, v60, v4
	v_mfma_f32_32x32x16_bf16 v[98:113], v[170:173], v[150:153], v[98:113]
	s_add_u32 s46, s46, s62
	s_addc_u32 s47, s47, s63
	s_and_b32 s64, s26, 3
	ds_read_b64_tr_b16 v[4:5], v3 offset:56320
	ds_read_b64_tr_b16 v[6:7], v3 offset:56832
	v_add_f32_e32 v3, v63, v16
	v_add_f32_e32 v16, v62, v17
	v_add_f32_e32 v3, v65, v3
	v_add_f32_e32 v16, v64, v16
	v_mfma_f32_32x32x16_bf16 v[114:129], v[178:181], v[154:157], v[114:129]
	s_mulk_i32 s64, 0x3000
	s_add_u32 s60, s60, 0x2000
	s_addc_u32 s61, s61, 0
	v_cvt_pk_bf16_f32 v178, v50, v51
	v_cvt_pk_bf16_f32 v179, v52, v53
	v_cvt_pk_bf16_f32 v186, v66, v67
	v_cvt_pk_bf16_f32 v187, v68, v69
	v_mfma_f32_32x32x16_bf16 v[98:113], v[166:169], v[154:157], v[98:113]
	s_add_i32 s52, s64, s91
	s_add_i32 s64, s42, 0x6000
	s_add_u32 s98, s98, s62
	s_addc_u32 s99, s99, s63
	v_cvt_pk_bf16_f32 v180, v54, v55
	v_cvt_pk_bf16_f32 v181, v56, v57
	v_cvt_pk_bf16_f32 v188, v70, v71
	v_cvt_pk_bf16_f32 v189, v72, v73
	v_mfma_f32_32x32x16_bf16 v[114:129], v[174:177], v[158:161], v[114:129]
	s_and_b32 s64, s64, 0x6000
	s_add_i32 s53, s64, s93
	v_cvt_pk_bf16_f32 v218, v58, v59
	v_cvt_pk_bf16_f32 v219, v60, v61
	v_cvt_pk_bf16_f32 v182, v74, v75
	v_cvt_pk_bf16_f32 v183, v76, v77
	v_mfma_f32_32x32x16_bf16 v[98:113], v[162:165], v[158:161], v[98:113]
	v_cvt_pk_bf16_f32 v220, v62, v63
	v_cvt_pk_bf16_f32 v221, v64, v65
	v_cvt_pk_bf16_f32 v184, v78, v79
	v_cvt_pk_bf16_f32 v185, v80, v81
	v_add_f32_e32 v3, v3, v16
	v_add_f32_e32 v246, v246, v3
	s_nop 3
	s_waitcnt lgkmcnt(0)
	v_mfma_f32_32x32x16_bf16 v[18:33], v[186:189], v[206:209], v[18:33]
	s_add_i32 s27, s26, 1
	s_and_b32 s64, s27, 3
	s_mulk_i32 s64, 0x3000
	v_exp_f32_e32 v66, v114
	v_exp_f32_e32 v67, v115
	v_exp_f32_e32 v68, v116
	v_exp_f32_e32 v69, v117
	v_add_u32_e32 v3, s64, v248
	v_mfma_f32_32x32x16_bf16 v[34:49], v[186:189], v[194:197], v[34:49]
	v_exp_f32_e32 v70, v118
	v_exp_f32_e32 v71, v119
	v_exp_f32_e32 v72, v120
	v_exp_f32_e32 v73, v121
	ds_read_b128 v[206:209], v3
	ds_read_b128 v[194:197], v3 offset:512
	v_mfma_f32_32x32x16_bf16 v[18:33], v[182:185], v[202:205], v[18:33]
	v_exp_f32_e32 v74, v122
	v_exp_f32_e32 v75, v123
	v_exp_f32_e32 v76, v124
	v_exp_f32_e32 v77, v125
	ds_read_b128 v[202:205], v3 offset:2048
	ds_read_b128 v[186:189], v3 offset:2560
	v_mfma_f32_32x32x16_bf16 v[34:49], v[182:185], v[214:217], v[34:49]
	v_exp_f32_e32 v78, v126
	v_exp_f32_e32 v79, v127
	v_exp_f32_e32 v80, v128
	v_exp_f32_e32 v81, v129
	ds_read_b128 v[198:201], v3 offset:4096
	ds_read_b128 v[182:185], v3 offset:4608
	v_mfma_f32_32x32x16_bf16 v[18:33], v[178:181], v[210:213], v[18:33]
	v_exp_f32_e32 v50, v98
	v_exp_f32_e32 v51, v99
	v_exp_f32_e32 v52, v100
	v_exp_f32_e32 v53, v101
	ds_read_b128 v[190:193], v3 offset:6144
	ds_read_b128 v[170:173], v3 offset:6656
	v_mfma_f32_32x32x16_bf16 v[34:49], v[178:181], v[12:15], v[34:49]
	v_exp_f32_e32 v54, v102
	v_exp_f32_e32 v55, v103
	v_exp_f32_e32 v56, v104
	v_exp_f32_e32 v57, v105
	ds_read_b128 v[178:181], v3 offset:8192
	ds_read_b128 v[166:169], v3 offset:8704
	v_mfma_f32_32x32x16_bf16 v[18:33], v[218:221], v[8:11], v[18:33]
	v_exp_f32_e32 v58, v106
	v_exp_f32_e32 v59, v107
	v_exp_f32_e32 v60, v108
	v_exp_f32_e32 v61, v109
	ds_read_b128 v[174:177], v3 offset:10240
	ds_read_b128 v[162:165], v3 offset:10752
	v_mfma_f32_32x32x16_bf16 v[34:49], v[218:221], v[4:7], v[34:49]
	v_exp_f32_e32 v62, v110
	v_exp_f32_e32 v63, v111
	v_exp_f32_e32 v64, v112
	v_exp_f32_e32 v65, v113
	s_mov_b32 s26, s27
	s_cmp_eq_u32 s27, s96
	s_cbranch_scc1 .Lmla_ss1_xdone
	s_add_i32 s64, s27, 3
	s_cmp_lt_u32 s64, s94
	s_cbranch_scc1 .Lmla_ss1_top
	s_waitcnt vmcnt(4)
	s_barrier
	s_branch .Lmla_ss_back

; template <bool FOX>
; __device__ __forceinline__ void attn_unit(const Args& A, int b, int h, int qb, LAS char* shm, LAS float* dg) {
;     ...
;     for (int t = 1; t < t_end; ++t) {
;         if (t == 1 && 4 < nti) ISSUE_K(t0 + 4, 0);
;         if (t + 4 < nti) ISSUE_K(t0 + t + 4, t % NS);
;         if (t + 2 < nti) ISSUE_V(t0 + t + 2, (t + 2) % NS);
;         SFENCE();
;         { if constexpr (!FOX) { if (t0 + t == tw_last + 1) {
; #pragma unroll
;                   for (int r = 0; r < 16; ++r) negm[r] = -INFINITY;
;                   asm volatile("" : "+v"(negm)); } }
;           const lds_cptr vp = vp0 + ((t - 1) % NS) * VSLOT; float sa = 0.f, sb = 0.f;
; #pragma unroll
;           for (int g = 0; g < 2 * NQ; ++g) {
;               if (!FOX && g == 0) c0 = __builtin_amdgcn_mfma_f32_32x32x16_bf16(kf[0], qr[0], negm, 0, 0, 0);
;               else if (!FOX && g == 1) c1 = __builtin_amdgcn_mfma_f32_32x32x16_bf16(kf[1], qr[0], negm, 0, 0, 0);
;               else if (g & 1) c1 = __builtin_amdgcn_mfma_f32_32x32x16_bf16(kf[g], qr[g >> 1], c1, 0, 0, 0); else c0 = __builtin_amdgcn_mfma_f32_32x32x16_bf16(kf[g], qr[g >> 1], c0, 0, 0, 0);
;               if (g < 8) { const int i = (g >> 1) + 4 * (g & 1); vlo[i] = vtr(vp + (i >> 2) * 4096 + (i & 3) * 1024); vhi[i] = vtr(vp + (i >> 2) * 4096 + (i & 3) * 1024 + 512);
;                   if (g < 4) { sa += pp0[4 * g]; sb += pp0[4 * g + 1]; sa += pp0[4 * g + 2]; sb += pp0[4 * g + 3]; } else { sa += pp1[4 * g - 16]; sb += pp1[4 * g - 15]; sa += pp1[4 * g - 14]; sb += pp1[4 * g - 13]; }
;                   asm volatile("" : "+v"(sa), "+v"(sb)); }
;               { constexpr int G0 = FOX ? 0 : 4; if (g >= G0) { const int q = 2 * (g - G0);
; #pragma unroll
;                   for (int k = 0; k < 2; ++k) { const int w = q + k; const unsigned pkd = w < 8 ? cvt_pk_bf16(pp0[2 * w], pp0[2 * w + 1]) : cvt_pk_bf16(pp1[2 * w - 16], pp1[2 * w - 15]); pw[w >> 2][w & 3] = pkd; } } }
;               SFENCE();
;           }
;           lrun += sa + sb; }
;         MASKONLY(t);
;         float rm; ROWMAX(rm);
;         bool resc = false;
;         if (__any(rm > THR)) { const float dl = fmaxf(rm, 0.f); mhat += dl;
; #pragma unroll
;             for (int r = 0; r < 16; ++r) { c0[r] -= dl; c1[r] -= dl; }
;             if constexpr (!FOX) {
; #pragma unroll
;                 for (int r = 0; r < 16; ++r) negm[r] = -mhat;
.Lmla_ss2_top:
	s_mov_b32 m0, s52
	s_nop 0
	global_load_lds_dwordx4 v240, s[46:47]
	s_mov_b32 m0, s53
	s_nop 0
	global_load_lds_dwordx4 v240, s[60:61]
	s_waitcnt lgkmcnt(0)
	s_add_i32 s27, s42, 0x8000
	v_mfma_f32_32x32x16_bf16 v[114:129], v[206:209], v[138:141], v[82:97]
	s_and_b32 s27, s27, 0x6000
	s_add_u32 s42, s42, 0x2000
	s_addc_u32 s43, s43, 0
	v_add_u32_e32 v3, s27, v247
	ds_read_b64_tr_b16 v[206:207], v3 offset:49152
	ds_read_b64_tr_b16 v[208:209], v3 offset:49664
	v_add_f32_e32 v4, v69, v67
	v_add_f32_e32 v5, v68, v66
	v_mfma_f32_32x32x16_bf16 v[98:113], v[194:197], v[138:141], v[82:97]
	ds_read_b64_tr_b16 v[194:195], v3 offset:53248
	ds_read_b64_tr_b16 v[196:197], v3 offset:53760
	v_add_f32_e32 v4, v71, v4
	v_add_f32_e32 v5, v70, v5
	v_add_f32_e32 v4, v73, v4
	v_add_f32_e32 v5, v72, v5
	v_mfma_f32_32x32x16_bf16 v[114:129], v[202:205], v[142:145], v[114:129]
	ds_read_b64_tr_b16 v[202:203], v3 offset:50176
	ds_read_b64_tr_b16 v[204:205], v3 offset:50688
	v_add_f32_e32 v4, v75, v4
	v_add_f32_e32 v5, v74, v5
	v_add_f32_e32 v4, v77, v4
	v_add_f32_e32 v5, v76, v5
	v_mfma_f32_32x32x16_bf16 v[98:113], v[186:189], v[142:145], v[98:113]
	ds_read_b64_tr_b16 v[214:215], v3 offset:54272
	ds_read_b64_tr_b16 v[216:217], v3 offset:54784
	v_add_f32_e32 v4, v79, v4
	v_add_f32_e32 v5, v78, v5
	v_add_f32_e32 v4, v81, v4
	v_add_f32_e32 v5, v80, v5
	v_mfma_f32_32x32x16_bf16 v[114:129], v[198:201], v[146:149], v[114:129]
	ds_read_b64_tr_b16 v[210:211], v3 offset:51200
	ds_read_b64_tr_b16 v[212:213], v3 offset:51712
	v_add_f32_e32 v4, v51, v4
	v_add_f32_e32 v5, v50, v5
	v_add_f32_e32 v4, v53, v4
	v_add_f32_e32 v5, v52, v5
	v_mfma_f32_32x32x16_bf16 v[98:113], v[182:185], v[146:149], v[98:113]
	ds_read_b64_tr_b16 v[12:13], v3 offset:55296
	ds_read_b64_tr_b16 v[14:15], v3 offset:55808
	v_add_f32_e32 v4, v55, v4
	v_add_f32_e32 v5, v54, v5
	v_add_f32_e32 v4, v57, v4
	v_add_f32_e32 v5, v56, v5
	v_mfma_f32_32x32x16_bf16 v[114:129], v[190:193], v[150:153], v[114:129]
	ds_read_b64_tr_b16 v[8:9], v3 offset:52224
	ds_read_b64_tr_b16 v[10:11], v3 offset:52736
	v_add_f32_e32 v4, v59, v4
	v_add_f32_e32 v16, v61, v4
	v_add_f32_e32 v4, v58, v5
	v_add_f32_e32 v17, v60, v4
	v_mfma_f32_32x32x16_bf16 v[98:113], v[170:173], v[150:153], v[98:113]
	s_add_u32 s46, s46, s62
	s_addc_u32 s47, s47, s63
	s_and_b32 s64, s26, 3
	ds_read_b64_tr_b16 v[4:5], v3 offset:56320
	ds_read_b64_tr_b16 v[6:7], v3 offset:56832
	v_add_f32_e32 v3, v63, v16
	v_add_f32_e32 v16, v62, v17
	v_add_f32_e32 v3, v65, v3
	v_add_f32_e32 v16, v64, v16
	v_mfma_f32_32x32x16_bf16 v[114:129], v[178:181], v[154:157], v[114:129]
	s_mulk_i32 s64, 0x3000
	s_add_u32 s60, s60, 0x2000
	s_addc_u32 s61, s61, 0
	v_cvt_pk_bf16_f32 v178, v50, v51
	v_cvt_pk_bf16_f32 v179, v52, v53
	v_cvt_pk_bf16_f32 v186, v66, v67
	v_cvt_pk_bf16_f32 v187, v68, v69
	v_mfma_f32_32x32x16_bf16 v[98:113], v[166:169], v[154:157], v[98:113]
	s_add_i32 s52, s64, s91
	s_add_i32 s64, s42, 0x6000
	v_cvt_pk_bf16_f32 v180, v54, v55
	v_cvt_pk_bf16_f32 v181, v56, v57
	v_cvt_pk_bf16_f32 v188, v70, v71
	v_cvt_pk_bf16_f32 v189, v72, v73
	v_mfma_f32_32x32x16_bf16 v[114:129], v[174:177], v[158:161], v[114:129]
	s_and_b32 s64, s64, 0x6000
	s_add_i32 s53, s64, s93
	v_cvt_pk_bf16_f32 v218, v58, v59
	v_cvt_pk_bf16_f32 v219, v60, v61
	v_cvt_pk_bf16_f32 v182, v74, v75
	v_cvt_pk_bf16_f32 v183, v76, v77
	v_mfma_f32_32x32x16_bf16 v[98:113], v[162:165], v[158:161], v[98:113]
	v_cvt_pk_bf16_f32 v220, v62, v63
	v_cvt_pk_bf16_f32 v221, v64, v65
	v_cvt_pk_bf16_f32 v184, v78, v79
	v_cvt_pk_bf16_f32 v185, v80, v81
	v_add_f32_e32 v3, v3, v16
	v_add_f32_e32 v246, v246, v3
	s_waitcnt vmcnt(3)
	s_waitcnt lgkmcnt(0)
	s_barrier
	v_mfma_f32_32x32x16_bf16 v[18:33], v[186:189], v[206:209], v[18:33]
	s_add_i32 s27, s26, 1
	s_and_b32 s64, s27, 3
	s_mulk_i32 s64, 0x3000
	v_exp_f32_e32 v66, v114
	v_exp_f32_e32 v67, v115
	v_exp_f32_e32 v68, v116
	v_exp_f32_e32 v69, v117
	v_add_u32_e32 v3, s64, v248
	v_mfma_f32_32x32x16_bf16 v[34:49], v[186:189], v[194:197], v[34:49]
	v_exp_f32_e32 v70, v118
	v_exp_f32_e32 v71, v119
	v_exp_f32_e32 v72, v120
	v_exp_f32_e32 v73, v121
	ds_read_b128 v[206:209], v3
	ds_read_b128 v[194:197], v3 offset:512
	v_mfma_f32_32x32x16_bf16 v[18:33], v[182:185], v[202:205], v[18:33]
	v_exp_f32_e32 v74, v122
	v_exp_f32_e32 v75, v123
	v_exp_f32_e32 v76, v124
	v_exp_f32_e32 v77, v125
	ds_read_b128 v[202:205], v3 offset:2048
	ds_read_b128 v[186:189], v3 offset:2560
	v_mfma_f32_32x32x16_bf16 v[34:49], v[182:185], v[214:217], v[34:49]
	v_exp_f32_e32 v78, v126
	v_exp_f32_e32 v79, v127
	v_exp_f32_e32 v80, v128
	v_exp_f32_e32 v81, v129
	ds_read_b128 v[198:201], v3 offset:4096
	ds_read_b128 v[182:185], v3 offset:4608
	v_mfma_f32_32x32x16_bf16 v[18:33], v[178:181], v[210:213], v[18:33]
	v_exp_f32_e32 v50, v98
	v_exp_f32_e32 v51, v99
	v_exp_f32_e32 v52, v100
	v_exp_f32_e32 v53, v101
	ds_read_b128 v[190:193], v3 offset:6144
	ds_read_b128 v[170:173], v3 offset:6656
	v_mfma_f32_32x32x16_bf16 v[34:49], v[178:181], v[12:15], v[34:49]
	v_exp_f32_e32 v54, v102
	v_exp_f32_e32 v55, v103
	v_exp_f32_e32 v56, v104
	v_exp_f32_e32 v57, v105
	ds_read_b128 v[178:181], v3 offset:8192
	ds_read_b128 v[166:169], v3 offset:8704
	v_mfma_f32_32x32x16_bf16 v[18:33], v[218:221], v[8:11], v[18:33]
	v_exp_f32_e32 v58, v106
	v_exp_f32_e32 v59, v107
	v_exp_f32_e32 v60, v108
	v_exp_f32_e32 v61, v109
	ds_read_b128 v[174:177], v3 offset:10240
	ds_read_b128 v[162:165], v3 offset:10752
	v_mfma_f32_32x32x16_bf16 v[34:49], v[218:221], v[4:7], v[34:49]
	v_exp_f32_e32 v62, v110
	v_exp_f32_e32 v63, v111
	v_exp_f32_e32 v64, v112
	v_exp_f32_e32 v65, v113
	s_mov_b32 s26, s27
	s_cmp_eq_u32 s27, s96
	s_cbranch_scc1 .Lmla_ss2_xdone
	s_add_i32 s64, s27, 3
	s_cmp_lt_u32 s64, s94
	s_cbranch_scc1 .Lmla_ss2_top
	s_branch .Lmla_ss_back
